# as previous plus nt (streaming) hint on the fp8 MoE weight stores of the conversion block (prologue and beside-GEMM converters)
# baseline (speedup 1.0000x reference)
.LBB0_10:
	v_ashrrev_i32_e32 v34, 31, v33
	v_lshrrev_b32_e32 v34, 28, v34
	v_add_u32_e32 v34, v33, v34
	v_ashrrev_i32_e32 v37, 4, v34
	v_lshlrev_b32_e32 v36, 5, v37
	v_mad_u64_u32 v[38:39], s[0:1], v37, s25, v[30:31]
	v_lshlrev_b32_e32 v86, 11, v37
	v_ashrrev_i32_e32 v37, 31, v36
	v_ashrrev_i32_e32 v39, 31, v38
	v_sub_u32_e32 v86, v32, v86
	v_lshl_add_u64 v[88:89], v[36:37], 2, v[28:29]
	v_ashrrev_i32_e32 v87, 31, v86
	v_lshl_add_u64 v[38:39], v[38:39], 2, v[88:89]
	v_lshl_add_u64 v[148:149], v[18:19], 0, v[86:87]
	v_add_co_u32_e64 v86, s[0:1], s26, v38
	v_ashrrev_i32_e32 v34, 6, v34
	s_nop 0
	v_addc_co_u32_e64 v87, s[0:1], 0, v39, s[0:1]
	v_add_co_u32_e64 v90, s[0:1], s27, v38
	v_ashrrev_i32_e32 v35, 31, v34
	s_nop 0
	v_addc_co_u32_e64 v91, s[0:1], 0, v39, s[0:1]
	v_add_co_u32_e64 v94, s[0:1], s28, v38
	v_lshlrev_b64 v[34:35], 8, v[34:35]
	s_nop 0
	v_addc_co_u32_e64 v95, s[0:1], 0, v39, s[0:1]
	v_add_co_u32_e64 v98, s[0:1], s22, v38
	v_lshl_add_u64 v[146:147], v[34:35], 0, s[14:15]
	s_nop 0
	v_addc_co_u32_e64 v99, s[0:1], 0, v39, s[0:1]
	v_add_co_u32_e64 v102, s[0:1], s29, v38
	v_and_or_b32 v154, v36, s24, v146
	s_nop 0
	v_addc_co_u32_e64 v103, s[0:1], 0, v39, s[0:1]
	v_add_co_u32_e64 v106, s[0:1], s30, v38
	global_load_dwordx4 v[34:37], v[38:39], off nt
	s_nop 0
	v_addc_co_u32_e64 v107, s[0:1], 0, v39, s[0:1]
	v_add_co_u32_e64 v110, s[0:1], s31, v38
	v_add_u32_e32 v71, 0x35a0, v40
	s_nop 0
	v_addc_co_u32_e64 v111, s[0:1], 0, v39, s[0:1]
	v_add_co_u32_e64 v114, s[0:1], s33, v38
	v_add_u32_e32 v73, 0x35a8, v40
	s_nop 0
	v_addc_co_u32_e64 v115, s[0:1], 0, v39, s[0:1]
	v_add_co_u32_e64 v118, s[0:1], s34, v38
	v_add_u32_e32 v76, 0x39c0, v40
	s_nop 0
	v_addc_co_u32_e64 v119, s[0:1], 0, v39, s[0:1]
	v_add_co_u32_e64 v122, s[0:1], s35, v38
	v_add_u32_e32 v77, 0x39c8, v40
	s_nop 0
	v_addc_co_u32_e64 v123, s[0:1], 0, v39, s[0:1]
	v_add_co_u32_e64 v126, s[0:1], s60, v38
	v_add_u32_e32 v82, 0x3de0, v40
	s_nop 0
	v_addc_co_u32_e64 v127, s[0:1], 0, v39, s[0:1]
	v_add_co_u32_e64 v130, s[0:1], s61, v38
	v_add_u32_e32 v83, 0x3de8, v40
	s_nop 0
	v_addc_co_u32_e64 v131, s[0:1], 0, v39, s[0:1]
	v_add_co_u32_e64 v134, s[0:1], s62, v38
	v_add_u32_e32 v84, 0x400, v75
	s_nop 0
	v_addc_co_u32_e64 v135, s[0:1], 0, v39, s[0:1]
	v_add_co_u32_e64 v138, s[0:1], s63, v38
	v_add_u32_e32 v85, 0x600, v75
	s_nop 0
	v_addc_co_u32_e64 v139, s[0:1], 0, v39, s[0:1]
	v_add_co_u32_e64 v38, s[0:1], s64, v38
	v_mov_b32_e32 v2, 0
	s_nop 0
	v_addc_co_u32_e64 v39, s[0:1], 0, v39, s[0:1]
	global_load_dwordx4 v[86:89], v[86:87], off nt
	s_nop 0
	global_load_dwordx4 v[90:93], v[90:91], off nt
	s_nop 0
	global_load_dwordx4 v[94:97], v[94:95], off nt
	s_nop 0
	global_load_dwordx4 v[98:101], v[98:99], off nt
	s_nop 0
	global_load_dwordx4 v[102:105], v[102:103], off nt
	s_nop 0
	global_load_dwordx4 v[106:109], v[106:107], off nt
	s_nop 0
	global_load_dwordx4 v[110:113], v[110:111], off nt
	s_nop 0
	global_load_dwordx4 v[114:117], v[114:115], off nt
	s_nop 0
	global_load_dwordx4 v[118:121], v[118:119], off nt
	s_nop 0
	global_load_dwordx4 v[122:125], v[122:123], off nt
	s_nop 0
	global_load_dwordx4 v[126:129], v[126:127], off nt
	s_nop 0
	global_load_dwordx4 v[130:133], v[130:131], off nt
	s_nop 0
	global_load_dwordx4 v[134:137], v[134:135], off nt
	s_nop 0
	global_load_dwordx4 v[138:141], v[138:139], off nt
	s_nop 0
	global_load_dwordx4 v[142:145], v[38:39], off nt
	v_mov_b32_e32 v3, 0
	v_mov_b32_e32 v4, 0
	v_mov_b32_e32 v5, 0
	v_mov_b32_e32 v6, 0
	v_mov_b32_e32 v7, 0
	v_mov_b32_e32 v8, 0
	v_mov_b32_e32 v9, 0
	v_mov_b32_e32 v10, 0
	v_mov_b32_e32 v11, 0
	v_mov_b32_e32 v12, 0
	v_mov_b32_e32 v13, 0
	v_mov_b32_e32 v14, 0
	v_mov_b32_e32 v15, 0
	v_mov_b32_e32 v16, 0
	v_mov_b32_e32 v17, 0
	v_or_b32_e32 v146, v154, v66
	v_lshlrev_b64 v[38:39], 11, v[146:147]
	v_or_b32_e32 v146, v154, v68
	v_lshlrev_b64 v[150:151], 11, v[146:147]
	v_or_b32_e32 v146, v154, v70
	v_lshlrev_b64 v[152:153], 11, v[146:147]
	v_or_b32_e32 v146, v154, v72
	v_lshl_add_u64 v[38:39], v[148:149], 0, v[38:39]
	v_lshlrev_b64 v[146:147], 11, v[146:147]
	v_lshl_add_u64 v[150:151], v[148:149], 0, v[150:151]
	v_lshl_add_u64 v[152:153], v[148:149], 0, v[152:153]
	s_waitcnt vmcnt(15)
	ds_write2_b32 v40, v34, v35 offset1:1
	ds_write2_b32 v40, v36, v37 offset0:2 offset1:3
	s_waitcnt vmcnt(14)
	ds_write2_b32 v41, v86, v87 offset1:1
	ds_write2_b32 v42, v88, v89 offset1:1
	s_waitcnt vmcnt(13)
	ds_write2_b32 v43, v90, v91 offset1:1
	ds_write2_b32 v44, v92, v93 offset1:1
	s_waitcnt vmcnt(12)
	ds_write2_b32 v45, v94, v95 offset1:1
	ds_write2_b32 v46, v96, v97 offset1:1
	s_waitcnt vmcnt(11)
	ds_write2_b32 v47, v98, v99 offset1:1
	ds_write2_b32 v48, v100, v101 offset1:1
	s_waitcnt vmcnt(10)
	ds_write2_b32 v49, v102, v103 offset1:1
	ds_write2_b32 v50, v104, v105 offset1:1
	s_waitcnt vmcnt(9)
	ds_write2_b32 v51, v106, v107 offset1:1
	ds_write2_b32 v52, v108, v109 offset1:1
	s_waitcnt vmcnt(8)
	ds_write2_b32 v53, v110, v111 offset1:1
	ds_write2_b32 v54, v112, v113 offset1:1
	s_waitcnt vmcnt(7)
	ds_write2_b32 v55, v114, v115 offset1:1
	ds_write2_b32 v56, v116, v117 offset1:1
	s_waitcnt vmcnt(6)
	ds_write2_b32 v57, v118, v119 offset1:1
	ds_write2_b32 v58, v120, v121 offset1:1
	s_waitcnt vmcnt(5)
	ds_write2_b32 v59, v122, v123 offset1:1
	ds_write2_b32 v60, v124, v125 offset1:1
	s_waitcnt vmcnt(4)
	ds_write2_b32 v61, v126, v127 offset1:1
	ds_write2_b32 v62, v128, v129 offset1:1
	s_waitcnt vmcnt(3)
	ds_write2_b32 v63, v130, v131 offset1:1
	ds_write2_b32 v64, v132, v133 offset1:1
	s_waitcnt vmcnt(2)
	ds_write2_b32 v71, v134, v135 offset1:1
	ds_write2_b32 v73, v136, v137 offset1:1
	s_waitcnt vmcnt(1)
	ds_write2_b32 v76, v138, v139 offset1:1
	ds_write2_b32 v77, v140, v141 offset1:1
	s_waitcnt vmcnt(0)
	ds_write2_b32 v82, v142, v143 offset1:1
	ds_write2_b32 v83, v144, v145 offset1:1
	s_waitcnt lgkmcnt(0)
	ds_read2_b32 v[34:35], v75 offset1:8
	ds_read2_b32 v[36:37], v75 offset0:33 offset1:41
	ds_read2_b32 v[86:87], v75 offset0:132 offset1:140
	ds_read2_b32 v[88:89], v75 offset0:165 offset1:173
	ds_read2_b32 v[90:91], v84 offset0:8 offset1:16
	ds_read2_b32 v[92:93], v84 offset0:41 offset1:49
	ds_read2_b32 v[94:95], v84 offset0:140 offset1:148
	ds_read2_b32 v[96:97], v84 offset0:173 offset1:181
	ds_read2_b32 v[98:99], v75 offset0:66 offset1:74
	ds_read2_b32 v[100:101], v75 offset0:99 offset1:107
	ds_read2_b32 v[102:103], v75 offset0:198 offset1:206
	ds_read2_b32 v[104:105], v75 offset0:231 offset1:239
	ds_read2_b32 v[106:107], v84 offset0:74 offset1:82
	ds_read2_b32 v[108:109], v84 offset0:107 offset1:115
	ds_read2_b32 v[110:111], v84 offset0:206 offset1:214
	ds_read2_b32 v[112:113], v84 offset0:239 offset1:247
	ds_read2_b32 v[114:115], v75 offset0:16 offset1:24
	ds_read2_b32 v[116:117], v75 offset0:49 offset1:57
	ds_read2_b32 v[118:119], v75 offset0:148 offset1:156
	ds_read2_b32 v[120:121], v75 offset0:181 offset1:189
	ds_read2_b32 v[122:123], v84 offset0:24 offset1:32
	ds_read2_b32 v[124:125], v84 offset0:57 offset1:65
	ds_read2_b32 v[126:127], v84 offset0:156 offset1:164
	ds_read2_b32 v[128:129], v84 offset0:189 offset1:197
	ds_read2_b32 v[130:131], v75 offset0:82 offset1:90
	ds_read2_b32 v[132:133], v75 offset0:115 offset1:123
	ds_read2_b32 v[134:135], v75 offset0:214 offset1:222
	ds_read2_b32 v[136:137], v75 offset0:247 offset1:255
	ds_read2_b32 v[138:139], v84 offset0:90 offset1:98
	ds_read2_b32 v[140:141], v84 offset0:123 offset1:131
	ds_read2_b32 v[142:143], v84 offset0:222 offset1:230
	ds_read2_b32 v[144:145], v85 offset0:127 offset1:135
	s_waitcnt lgkmcnt(14)
	v_mul_f32_e32 v34, 0x43800000, v34
	v_mul_f32_e32 v36, 0x43800000, v36
	v_mul_f32_e32 v86, 0x43800000, v86
	v_mul_f32_e32 v88, 0x43800000, v88
	v_mul_f32_e32 v90, 0x43800000, v90
	v_mul_f32_e32 v92, 0x43800000, v92
	v_mul_f32_e32 v94, 0x43800000, v94
	v_mul_f32_e32 v96, 0x43800000, v96
	v_mul_f32_e32 v35, 0x43800000, v35
	v_mul_f32_e32 v37, 0x43800000, v37
	v_mul_f32_e32 v87, 0x43800000, v87
	v_mul_f32_e32 v89, 0x43800000, v89
	v_mul_f32_e32 v91, 0x43800000, v91
	v_mul_f32_e32 v93, 0x43800000, v93
	v_mul_f32_e32 v95, 0x43800000, v95
	v_mul_f32_e32 v97, 0x43800000, v97
	v_med3_f32 v34, v34, s65, v65
	v_med3_f32 v36, v36, s65, v65
	v_med3_f32 v86, v86, s65, v65
	v_med3_f32 v88, v88, s65, v65
	v_med3_f32 v90, v90, s65, v65
	v_med3_f32 v92, v92, s65, v65
	v_med3_f32 v94, v94, s65, v65
	v_med3_f32 v96, v96, s65, v65
	v_mul_f32_e32 v114, 0x43800000, v114
	v_mul_f32_e32 v116, 0x43800000, v116
	s_waitcnt lgkmcnt(13)
	v_mul_f32_e32 v118, 0x43800000, v118
	s_waitcnt lgkmcnt(12)
	v_mul_f32_e32 v120, 0x43800000, v120
	s_waitcnt lgkmcnt(11)
	v_mul_f32_e32 v122, 0x43800000, v122
	s_waitcnt lgkmcnt(10)
	v_mul_f32_e32 v124, 0x43800000, v124
	s_waitcnt lgkmcnt(9)
	v_mul_f32_e32 v126, 0x43800000, v126
	s_waitcnt lgkmcnt(8)
	v_mul_f32_e32 v128, 0x43800000, v128
	v_med3_f32 v35, v35, s65, v65
	v_med3_f32 v37, v37, s65, v65
	v_med3_f32 v87, v87, s65, v65
	v_med3_f32 v89, v89, s65, v65
	v_med3_f32 v91, v91, s65, v65
	v_med3_f32 v93, v93, s65, v65
	v_med3_f32 v95, v95, s65, v65
	v_med3_f32 v97, v97, s65, v65
	v_cvt_pk_fp8_f32 v2, v34, v36
	v_cvt_pk_fp8_f32 v3, v86, v88
	v_cvt_pk_fp8_f32 v4, v90, v92
	v_cvt_pk_fp8_f32 v5, v94, v96
	v_mul_f32_e32 v115, 0x43800000, v115
	v_mul_f32_e32 v117, 0x43800000, v117
	v_mul_f32_e32 v119, 0x43800000, v119
	v_mul_f32_e32 v121, 0x43800000, v121
	v_mul_f32_e32 v123, 0x43800000, v123
	v_mul_f32_e32 v125, 0x43800000, v125
	v_mul_f32_e32 v127, 0x43800000, v127
	v_mul_f32_e32 v129, 0x43800000, v129
	v_med3_f32 v114, v114, s65, v65
	v_med3_f32 v116, v116, s65, v65
	v_med3_f32 v118, v118, s65, v65
	v_med3_f32 v120, v120, s65, v65
	v_med3_f32 v122, v122, s65, v65
	v_med3_f32 v124, v124, s65, v65
	v_med3_f32 v126, v126, s65, v65
	v_med3_f32 v128, v128, s65, v65
	v_cvt_pk_fp8_f32 v6, v35, v37
	v_cvt_pk_fp8_f32 v7, v87, v89
	v_cvt_pk_fp8_f32 v8, v91, v93
	v_cvt_pk_fp8_f32 v9, v95, v97
	v_mul_f32_e32 v98, 0x43800000, v98
	v_mul_f32_e32 v100, 0x43800000, v100
	v_mul_f32_e32 v102, 0x43800000, v102
	v_mul_f32_e32 v104, 0x43800000, v104
	v_mul_f32_e32 v106, 0x43800000, v106
	v_mul_f32_e32 v108, 0x43800000, v108
	v_mul_f32_e32 v110, 0x43800000, v110
	v_mul_f32_e32 v112, 0x43800000, v112
	v_med3_f32 v115, v115, s65, v65
	v_med3_f32 v117, v117, s65, v65
	v_med3_f32 v119, v119, s65, v65
	v_med3_f32 v121, v121, s65, v65
	v_med3_f32 v123, v123, s65, v65
	v_med3_f32 v125, v125, s65, v65
	v_med3_f32 v127, v127, s65, v65
	v_med3_f32 v129, v129, s65, v65
	v_cvt_pk_fp8_f32 v10, v114, v116
	v_cvt_pk_fp8_f32 v11, v118, v120
	v_cvt_pk_fp8_f32 v12, v122, v124
	v_cvt_pk_fp8_f32 v13, v126, v128
	v_mul_f32_e32 v99, 0x43800000, v99
	v_mul_f32_e32 v101, 0x43800000, v101
	v_mul_f32_e32 v103, 0x43800000, v103
	v_mul_f32_e32 v105, 0x43800000, v105
	v_mul_f32_e32 v107, 0x43800000, v107
	v_mul_f32_e32 v109, 0x43800000, v109
	v_mul_f32_e32 v111, 0x43800000, v111
	v_mul_f32_e32 v113, 0x43800000, v113
	v_med3_f32 v98, v98, s65, v65
	v_med3_f32 v100, v100, s65, v65
	v_med3_f32 v102, v102, s65, v65
	v_med3_f32 v104, v104, s65, v65
	v_med3_f32 v106, v106, s65, v65
	v_med3_f32 v108, v108, s65, v65
	v_med3_f32 v110, v110, s65, v65
	v_med3_f32 v112, v112, s65, v65
	v_cvt_pk_fp8_f32 v14, v115, v117
	v_cvt_pk_fp8_f32 v15, v119, v121
	v_cvt_pk_fp8_f32 v16, v123, v125
	v_cvt_pk_fp8_f32 v17, v127, v129
	s_waitcnt lgkmcnt(7)
	v_mul_f32_e32 v130, 0x43800000, v130
	s_waitcnt lgkmcnt(6)
	v_mul_f32_e32 v132, 0x43800000, v132
	s_waitcnt lgkmcnt(5)
	v_mul_f32_e32 v134, 0x43800000, v134
	s_waitcnt lgkmcnt(4)
	v_mul_f32_e32 v136, 0x43800000, v136
	s_waitcnt lgkmcnt(3)
	v_mul_f32_e32 v138, 0x43800000, v138
	s_waitcnt lgkmcnt(2)
	v_mul_f32_e32 v140, 0x43800000, v140
	s_waitcnt lgkmcnt(1)
	v_mul_f32_e32 v142, 0x43800000, v142
	s_waitcnt lgkmcnt(0)
	v_mul_f32_e32 v144, 0x43800000, v144
	v_med3_f32 v99, v99, s65, v65
	v_med3_f32 v101, v101, s65, v65
	v_med3_f32 v103, v103, s65, v65
	v_med3_f32 v105, v105, s65, v65
	v_med3_f32 v107, v107, s65, v65
	v_med3_f32 v109, v109, s65, v65
	v_med3_f32 v111, v111, s65, v65
	v_med3_f32 v113, v113, s65, v65
	v_cvt_pk_fp8_f32 v2, v98, v100 op_sel:[0,0,1]
	v_cvt_pk_fp8_f32 v3, v102, v104 op_sel:[0,0,1]
	v_cvt_pk_fp8_f32 v4, v106, v108 op_sel:[0,0,1]
	v_cvt_pk_fp8_f32 v5, v110, v112 op_sel:[0,0,1]
	v_mul_f32_e32 v131, 0x43800000, v131
	v_mul_f32_e32 v133, 0x43800000, v133
	v_mul_f32_e32 v135, 0x43800000, v135
	v_mul_f32_e32 v137, 0x43800000, v137
	v_mul_f32_e32 v139, 0x43800000, v139
	v_mul_f32_e32 v141, 0x43800000, v141
	v_mul_f32_e32 v143, 0x43800000, v143
	v_mul_f32_e32 v145, 0x43800000, v145
	v_med3_f32 v130, v130, s65, v65
	v_med3_f32 v132, v132, s65, v65
	v_med3_f32 v134, v134, s65, v65
	v_med3_f32 v136, v136, s65, v65
	v_med3_f32 v138, v138, s65, v65
	v_med3_f32 v140, v140, s65, v65
	v_med3_f32 v142, v142, s65, v65
	v_med3_f32 v144, v144, s65, v65
	v_cvt_pk_fp8_f32 v6, v99, v101 op_sel:[0,0,1]
	v_cvt_pk_fp8_f32 v7, v103, v105 op_sel:[0,0,1]
	v_cvt_pk_fp8_f32 v8, v107, v109 op_sel:[0,0,1]
	v_cvt_pk_fp8_f32 v9, v111, v113 op_sel:[0,0,1]
	v_med3_f32 v131, v131, s65, v65
	v_med3_f32 v133, v133, s65, v65
	v_med3_f32 v135, v135, s65, v65
	v_med3_f32 v137, v137, s65, v65
	v_med3_f32 v139, v139, s65, v65
	v_med3_f32 v141, v141, s65, v65
	v_med3_f32 v143, v143, s65, v65
	v_med3_f32 v145, v145, s65, v65
	v_cvt_pk_fp8_f32 v10, v130, v132 op_sel:[0,0,1]
	v_cvt_pk_fp8_f32 v11, v134, v136 op_sel:[0,0,1]
	v_cvt_pk_fp8_f32 v12, v138, v140 op_sel:[0,0,1]
	v_cvt_pk_fp8_f32 v13, v142, v144 op_sel:[0,0,1]
	v_cvt_pk_fp8_f32 v14, v131, v133 op_sel:[0,0,1]
	v_cvt_pk_fp8_f32 v15, v135, v137 op_sel:[0,0,1]
	v_cvt_pk_fp8_f32 v16, v139, v141 op_sel:[0,0,1]
	v_cvt_pk_fp8_f32 v17, v143, v145 op_sel:[0,0,1]
	v_lshl_add_u64 v[146:147], v[148:149], 0, v[146:147]
	global_store_dwordx4 v[38:39], v[2:5], off nt
	global_store_dwordx4 v[150:151], v[6:9], off nt
	global_store_dwordx4 v[152:153], v[10:13], off nt
	global_store_dwordx4 v[146:147], v[14:17], off nt
	v_add_u32_e32 v33, s3, v33
	s_waitcnt lgkmcnt(0)
	v_cmp_lt_i32_e64 s[6:7], s66, v33
	v_add_u32_e32 v30, s23, v30
	s_or_b64 s[18:19], s[6:7], s[18:19]
	v_add_u32_e32 v32, s67, v32
	s_andn2_b64 exec, exec, s[18:19]
	s_cbranch_execnz .LBB0_10
	s_or_b64 exec, exec, s[18:19]
	s_bitset1_b32 s14, 7
	v_lshl_add_u64 v[28:29], s[16:17], 2, v[24:25]
	s_mov_b64 s[16:17], 0
	v_mov_b32_e32 v86, v74
	v_mov_b32_e32 v30, v1
	v_mov_b32_e32 v87, v69
.LBB0_12:
	v_ashrrev_i32_e32 v32, 31, v87
	v_lshrrev_b32_e32 v32, 28, v32
	v_add_u32_e32 v32, v87, v32
	v_ashrrev_i32_e32 v33, 4, v32
	v_ashrrev_i32_e32 v32, 6, v32
	v_lshlrev_b32_e32 v34, 5, v33
	v_mad_u64_u32 v[36:37], s[0:1], v33, s25, v[30:31]
	v_lshlrev_b32_e32 v38, 11, v33
	v_ashrrev_i32_e32 v33, 31, v32
	v_ashrrev_i32_e32 v35, 31, v34
	v_ashrrev_i32_e32 v37, 31, v36
	v_lshlrev_b64 v[32:33], 8, v[32:33]
	v_lshl_add_u64 v[88:89], v[34:35], 2, v[28:29]
	v_lshl_add_u64 v[152:153], s[14:15], 0, v[32:33]
	v_lshl_add_u64 v[32:33], v[36:37], 2, v[88:89]
	v_and_or_b32 v154, v34, s24, v152
	v_add_co_u32_e64 v34, s[0:1], s26, v32
	global_load_dwordx4 v[88:91], v[32:33], off nt
	s_nop 0
	v_addc_co_u32_e64 v35, s[0:1], 0, v33, s[0:1]
	v_add_co_u32_e64 v36, s[0:1], s27, v32
	v_mov_b32_e32 v2, 0
	s_nop 0
	v_addc_co_u32_e64 v37, s[0:1], 0, v33, s[0:1]
	v_add_co_u32_e64 v100, s[0:1], s28, v32
	v_mov_b32_e32 v3, 0
	s_nop 0
	v_addc_co_u32_e64 v101, s[0:1], 0, v33, s[0:1]
	v_add_co_u32_e64 v104, s[0:1], s22, v32
	v_mov_b32_e32 v4, 0
	s_nop 0
	v_addc_co_u32_e64 v105, s[0:1], 0, v33, s[0:1]
	v_add_co_u32_e64 v108, s[0:1], s29, v32
	v_mov_b32_e32 v5, 0
	s_nop 0
	v_addc_co_u32_e64 v109, s[0:1], 0, v33, s[0:1]
	v_add_co_u32_e64 v112, s[0:1], s30, v32
	v_mov_b32_e32 v6, 0
	s_nop 0
	v_addc_co_u32_e64 v113, s[0:1], 0, v33, s[0:1]
	v_add_co_u32_e64 v116, s[0:1], s31, v32
	v_mov_b32_e32 v7, 0
	s_nop 0
	v_addc_co_u32_e64 v117, s[0:1], 0, v33, s[0:1]
	v_add_co_u32_e64 v120, s[0:1], s33, v32
	v_mov_b32_e32 v8, 0
	s_nop 0
	v_addc_co_u32_e64 v121, s[0:1], 0, v33, s[0:1]
	v_add_co_u32_e64 v124, s[0:1], s34, v32
	v_mov_b32_e32 v9, 0
	s_nop 0
	v_addc_co_u32_e64 v125, s[0:1], 0, v33, s[0:1]
	v_add_co_u32_e64 v128, s[0:1], s35, v32
	v_mov_b32_e32 v10, 0
	s_nop 0
	v_addc_co_u32_e64 v129, s[0:1], 0, v33, s[0:1]
	v_add_co_u32_e64 v132, s[0:1], s60, v32
	v_mov_b32_e32 v11, 0
	s_nop 0
	v_addc_co_u32_e64 v133, s[0:1], 0, v33, s[0:1]
	v_add_co_u32_e64 v136, s[0:1], s61, v32
	v_mov_b32_e32 v12, 0
	s_nop 0
	v_addc_co_u32_e64 v137, s[0:1], 0, v33, s[0:1]
	v_add_co_u32_e64 v140, s[0:1], s62, v32
	v_mov_b32_e32 v13, 0
	s_nop 0
	v_addc_co_u32_e64 v141, s[0:1], 0, v33, s[0:1]
	v_add_co_u32_e64 v144, s[0:1], s63, v32
	v_mov_b32_e32 v14, 0
	s_nop 0
	v_addc_co_u32_e64 v145, s[0:1], 0, v33, s[0:1]
	v_add_co_u32_e64 v32, s[0:1], s64, v32
	v_mov_b32_e32 v15, 0
	s_nop 0
	v_addc_co_u32_e64 v33, s[0:1], 0, v33, s[0:1]
	global_load_dwordx4 v[92:95], v[34:35], off nt
	global_load_dwordx4 v[96:99], v[36:37], off nt
	s_nop 0
	global_load_dwordx4 v[100:103], v[100:101], off nt
	s_nop 0
	global_load_dwordx4 v[104:107], v[104:105], off nt
	s_nop 0
	global_load_dwordx4 v[108:111], v[108:109], off nt
	s_nop 0
	global_load_dwordx4 v[112:115], v[112:113], off nt
	s_nop 0
	global_load_dwordx4 v[116:119], v[116:117], off nt
	s_nop 0
	global_load_dwordx4 v[120:123], v[120:121], off nt
	s_nop 0
	global_load_dwordx4 v[124:127], v[124:125], off nt
	s_nop 0
	global_load_dwordx4 v[128:131], v[128:129], off nt
	s_nop 0
	global_load_dwordx4 v[132:135], v[132:133], off nt
	s_nop 0
	global_load_dwordx4 v[136:139], v[136:137], off nt
	s_nop 0
	global_load_dwordx4 v[140:143], v[140:141], off nt
	s_nop 0
	global_load_dwordx4 v[144:147], v[144:145], off nt
	s_nop 0
	global_load_dwordx4 v[148:151], v[32:33], off nt
	v_mov_b32_e32 v16, 0
	v_mov_b32_e32 v17, 0
	v_or_b32_e32 v152, v154, v66
	v_sub_u32_e32 v38, v86, v38
	v_lshlrev_b64 v[32:33], 11, v[152:153]
	v_or_b32_e32 v152, v154, v68
	v_ashrrev_i32_e32 v39, 31, v38
	v_lshlrev_b64 v[34:35], 11, v[152:153]
	v_or_b32_e32 v152, v154, v70
	v_lshl_add_u64 v[38:39], v[18:19], 0, v[38:39]
	v_lshlrev_b64 v[36:37], 11, v[152:153]
	v_or_b32_e32 v152, v154, v72
	v_lshl_add_u64 v[32:33], v[38:39], 0, v[32:33]
	v_lshlrev_b64 v[152:153], 11, v[152:153]
	v_lshl_add_u64 v[34:35], v[38:39], 0, v[34:35]
	v_lshl_add_u64 v[36:37], v[38:39], 0, v[36:37]
	v_lshl_add_u64 v[38:39], v[38:39], 0, v[152:153]
	v_add_u32_e32 v87, s3, v87
	v_cmp_lt_i32_e64 s[6:7], s66, v87
	v_add_u32_e32 v30, s23, v30
	s_or_b64 s[16:17], s[6:7], s[16:17]
	v_add_u32_e32 v86, s67, v86
	s_waitcnt vmcnt(15)
	ds_write2_b32 v40, v88, v89 offset1:1
	ds_write2_b32 v40, v90, v91 offset0:2 offset1:3
	s_waitcnt vmcnt(14)
	ds_write2_b32 v41, v92, v93 offset1:1
	ds_write2_b32 v42, v94, v95 offset1:1
	s_waitcnt vmcnt(13)
	ds_write2_b32 v43, v96, v97 offset1:1
	ds_write2_b32 v44, v98, v99 offset1:1
	s_waitcnt vmcnt(12)
	ds_write2_b32 v45, v100, v101 offset1:1
	ds_write2_b32 v46, v102, v103 offset1:1
	s_waitcnt vmcnt(11)
	ds_write2_b32 v47, v104, v105 offset1:1
	ds_write2_b32 v48, v106, v107 offset1:1
	s_waitcnt vmcnt(10)
	ds_write2_b32 v49, v108, v109 offset1:1
	ds_write2_b32 v50, v110, v111 offset1:1
	s_waitcnt vmcnt(9)
	ds_write2_b32 v51, v112, v113 offset1:1
	ds_write2_b32 v52, v114, v115 offset1:1
	s_waitcnt vmcnt(8)
	ds_write2_b32 v53, v116, v117 offset1:1
	ds_write2_b32 v54, v118, v119 offset1:1
	s_waitcnt vmcnt(7)
	ds_write2_b32 v55, v120, v121 offset1:1
	ds_write2_b32 v56, v122, v123 offset1:1
	s_waitcnt vmcnt(6)
	ds_write2_b32 v57, v124, v125 offset1:1
	ds_write2_b32 v58, v126, v127 offset1:1
	s_waitcnt vmcnt(5)
	ds_write2_b32 v59, v128, v129 offset1:1
	ds_write2_b32 v60, v130, v131 offset1:1
	s_waitcnt vmcnt(4)
	ds_write2_b32 v61, v132, v133 offset1:1
	ds_write2_b32 v62, v134, v135 offset1:1
	s_waitcnt vmcnt(3)
	ds_write2_b32 v63, v136, v137 offset1:1
	ds_write2_b32 v64, v138, v139 offset1:1
	s_waitcnt vmcnt(2)
	ds_write2_b32 v71, v140, v141 offset1:1
	ds_write2_b32 v73, v142, v143 offset1:1
	s_waitcnt vmcnt(1)
	ds_write2_b32 v76, v144, v145 offset1:1
	ds_write2_b32 v77, v146, v147 offset1:1
	s_waitcnt vmcnt(0)
	ds_write2_b32 v82, v148, v149 offset1:1
	ds_write2_b32 v83, v150, v151 offset1:1
	s_waitcnt lgkmcnt(0)
	ds_read2_b32 v[88:89], v75 offset1:8
	ds_read2_b32 v[90:91], v75 offset0:33 offset1:41
	ds_read2_b32 v[92:93], v75 offset0:66 offset1:74
	ds_read2_b32 v[94:95], v75 offset0:99 offset1:107
	ds_read2_b32 v[96:97], v75 offset0:132 offset1:140
	ds_read2_b32 v[98:99], v75 offset0:165 offset1:173
	ds_read2_b32 v[100:101], v84 offset0:8 offset1:16
	ds_read2_b32 v[102:103], v84 offset0:41 offset1:49
	ds_read2_b32 v[104:105], v84 offset0:140 offset1:148
	ds_read2_b32 v[106:107], v84 offset0:173 offset1:181
	ds_read2_b32 v[108:109], v75 offset0:16 offset1:24
	ds_read2_b32 v[110:111], v75 offset0:49 offset1:57
	ds_read2_b32 v[112:113], v75 offset0:148 offset1:156
	ds_read2_b32 v[114:115], v75 offset0:181 offset1:189
	ds_read2_b32 v[116:117], v84 offset0:24 offset1:32
	ds_read2_b32 v[118:119], v84 offset0:57 offset1:65
	ds_read2_b32 v[120:121], v84 offset0:156 offset1:164
	ds_read2_b32 v[122:123], v84 offset0:189 offset1:197
	ds_read2_b32 v[124:125], v75 offset0:198 offset1:206
	ds_read2_b32 v[126:127], v75 offset0:231 offset1:239
	ds_read2_b32 v[128:129], v84 offset0:74 offset1:82
	ds_read2_b32 v[130:131], v84 offset0:107 offset1:115
	ds_read2_b32 v[132:133], v84 offset0:206 offset1:214
	ds_read2_b32 v[134:135], v84 offset0:239 offset1:247
	ds_read2_b32 v[136:137], v75 offset0:82 offset1:90
	ds_read2_b32 v[138:139], v75 offset0:115 offset1:123
	ds_read2_b32 v[140:141], v75 offset0:214 offset1:222
	ds_read2_b32 v[142:143], v75 offset0:247 offset1:255
	ds_read2_b32 v[144:145], v84 offset0:90 offset1:98
	ds_read2_b32 v[146:147], v84 offset0:123 offset1:131
	ds_read2_b32 v[148:149], v84 offset0:222 offset1:230
	ds_read2_b32 v[150:151], v85 offset0:127 offset1:135
	s_waitcnt lgkmcnt(14)
	v_mul_f32_e32 v88, 0x43800000, v88
	v_mul_f32_e32 v90, 0x43800000, v90
	v_mul_f32_e32 v96, 0x43800000, v96
	v_mul_f32_e32 v98, 0x43800000, v98
	v_mul_f32_e32 v100, 0x43800000, v100
	v_mul_f32_e32 v102, 0x43800000, v102
	v_mul_f32_e32 v104, 0x43800000, v104
	v_mul_f32_e32 v106, 0x43800000, v106
	v_mul_f32_e32 v89, 0x43800000, v89
	v_mul_f32_e32 v91, 0x43800000, v91
	v_mul_f32_e32 v97, 0x43800000, v97
	v_mul_f32_e32 v99, 0x43800000, v99
	v_mul_f32_e32 v101, 0x43800000, v101
	v_mul_f32_e32 v103, 0x43800000, v103
	v_mul_f32_e32 v105, 0x43800000, v105
	v_mul_f32_e32 v107, 0x43800000, v107
	v_med3_f32 v88, v88, s65, v65
	v_med3_f32 v90, v90, s65, v65
	v_med3_f32 v96, v96, s65, v65
	v_med3_f32 v98, v98, s65, v65
	v_med3_f32 v100, v100, s65, v65
	v_med3_f32 v102, v102, s65, v65
	v_med3_f32 v104, v104, s65, v65
	v_med3_f32 v106, v106, s65, v65
	v_mul_f32_e32 v108, 0x43800000, v108
	v_mul_f32_e32 v110, 0x43800000, v110
	v_mul_f32_e32 v112, 0x43800000, v112
	v_mul_f32_e32 v114, 0x43800000, v114
	v_mul_f32_e32 v116, 0x43800000, v116
	v_mul_f32_e32 v118, 0x43800000, v118
	v_mul_f32_e32 v120, 0x43800000, v120
	v_mul_f32_e32 v122, 0x43800000, v122
	v_med3_f32 v89, v89, s65, v65
	v_med3_f32 v91, v91, s65, v65
	v_med3_f32 v97, v97, s65, v65
	v_med3_f32 v99, v99, s65, v65
	v_med3_f32 v101, v101, s65, v65
	v_med3_f32 v103, v103, s65, v65
	v_med3_f32 v105, v105, s65, v65
	v_med3_f32 v107, v107, s65, v65
	v_cvt_pk_fp8_f32 v2, v88, v90
	v_cvt_pk_fp8_f32 v3, v96, v98
	v_cvt_pk_fp8_f32 v4, v100, v102
	v_cvt_pk_fp8_f32 v5, v104, v106
	v_mul_f32_e32 v109, 0x43800000, v109
	v_mul_f32_e32 v111, 0x43800000, v111
	v_mul_f32_e32 v113, 0x43800000, v113
	v_mul_f32_e32 v115, 0x43800000, v115
	v_mul_f32_e32 v117, 0x43800000, v117
	v_mul_f32_e32 v119, 0x43800000, v119
	v_mul_f32_e32 v121, 0x43800000, v121
	v_mul_f32_e32 v123, 0x43800000, v123
	v_med3_f32 v108, v108, s65, v65
	v_med3_f32 v110, v110, s65, v65
	v_med3_f32 v112, v112, s65, v65
	v_med3_f32 v114, v114, s65, v65
	v_med3_f32 v116, v116, s65, v65
	v_med3_f32 v118, v118, s65, v65
	v_med3_f32 v120, v120, s65, v65
	v_med3_f32 v122, v122, s65, v65
	v_cvt_pk_fp8_f32 v6, v89, v91
	v_cvt_pk_fp8_f32 v7, v97, v99
	v_cvt_pk_fp8_f32 v8, v101, v103
	v_cvt_pk_fp8_f32 v9, v105, v107
	v_mul_f32_e32 v92, 0x43800000, v92
	v_mul_f32_e32 v94, 0x43800000, v94
	s_waitcnt lgkmcnt(13)
	v_mul_f32_e32 v124, 0x43800000, v124
	s_waitcnt lgkmcnt(12)
	v_mul_f32_e32 v126, 0x43800000, v126
	s_waitcnt lgkmcnt(11)
	v_mul_f32_e32 v128, 0x43800000, v128
	s_waitcnt lgkmcnt(10)
	v_mul_f32_e32 v130, 0x43800000, v130
	s_waitcnt lgkmcnt(9)
	v_mul_f32_e32 v132, 0x43800000, v132
	s_waitcnt lgkmcnt(8)
	v_mul_f32_e32 v134, 0x43800000, v134
	v_med3_f32 v109, v109, s65, v65
	v_med3_f32 v111, v111, s65, v65
	v_med3_f32 v113, v113, s65, v65
	v_med3_f32 v115, v115, s65, v65
	v_med3_f32 v117, v117, s65, v65
	v_med3_f32 v119, v119, s65, v65
	v_med3_f32 v121, v121, s65, v65
	v_med3_f32 v123, v123, s65, v65
	v_cvt_pk_fp8_f32 v10, v108, v110
	v_cvt_pk_fp8_f32 v11, v112, v114
	v_cvt_pk_fp8_f32 v12, v116, v118
	v_cvt_pk_fp8_f32 v13, v120, v122
	v_mul_f32_e32 v93, 0x43800000, v93
	v_mul_f32_e32 v95, 0x43800000, v95
	v_mul_f32_e32 v125, 0x43800000, v125
	v_mul_f32_e32 v127, 0x43800000, v127
	v_mul_f32_e32 v129, 0x43800000, v129
	v_mul_f32_e32 v131, 0x43800000, v131
	v_mul_f32_e32 v133, 0x43800000, v133
	v_mul_f32_e32 v135, 0x43800000, v135
	v_med3_f32 v92, v92, s65, v65
	v_med3_f32 v94, v94, s65, v65
	v_med3_f32 v124, v124, s65, v65
	v_med3_f32 v126, v126, s65, v65
	v_med3_f32 v128, v128, s65, v65
	v_med3_f32 v130, v130, s65, v65
	v_med3_f32 v132, v132, s65, v65
	v_med3_f32 v134, v134, s65, v65
	v_cvt_pk_fp8_f32 v14, v109, v111
	v_cvt_pk_fp8_f32 v15, v113, v115
	v_cvt_pk_fp8_f32 v16, v117, v119
	v_cvt_pk_fp8_f32 v17, v121, v123
	s_waitcnt lgkmcnt(7)
	v_mul_f32_e32 v136, 0x43800000, v136
	s_waitcnt lgkmcnt(6)
	v_mul_f32_e32 v138, 0x43800000, v138
	s_waitcnt lgkmcnt(5)
	v_mul_f32_e32 v140, 0x43800000, v140
	s_waitcnt lgkmcnt(4)
	v_mul_f32_e32 v142, 0x43800000, v142
	s_waitcnt lgkmcnt(3)
	v_mul_f32_e32 v144, 0x43800000, v144
	s_waitcnt lgkmcnt(2)
	v_mul_f32_e32 v146, 0x43800000, v146
	s_waitcnt lgkmcnt(1)
	v_mul_f32_e32 v148, 0x43800000, v148
	s_waitcnt lgkmcnt(0)
	v_mul_f32_e32 v150, 0x43800000, v150
	v_med3_f32 v93, v93, s65, v65
	v_med3_f32 v95, v95, s65, v65
	v_med3_f32 v125, v125, s65, v65
	v_med3_f32 v127, v127, s65, v65
	v_med3_f32 v129, v129, s65, v65
	v_med3_f32 v131, v131, s65, v65
	v_med3_f32 v133, v133, s65, v65
	v_med3_f32 v135, v135, s65, v65
	v_cvt_pk_fp8_f32 v2, v92, v94 op_sel:[0,0,1]
	v_cvt_pk_fp8_f32 v3, v124, v126 op_sel:[0,0,1]
	v_cvt_pk_fp8_f32 v4, v128, v130 op_sel:[0,0,1]
	v_cvt_pk_fp8_f32 v5, v132, v134 op_sel:[0,0,1]
	v_mul_f32_e32 v137, 0x43800000, v137
	v_mul_f32_e32 v139, 0x43800000, v139
	v_mul_f32_e32 v141, 0x43800000, v141
	v_mul_f32_e32 v143, 0x43800000, v143
	v_mul_f32_e32 v145, 0x43800000, v145
	v_mul_f32_e32 v147, 0x43800000, v147
	v_mul_f32_e32 v149, 0x43800000, v149
	v_mul_f32_e32 v151, 0x43800000, v151
	v_med3_f32 v136, v136, s65, v65
	v_med3_f32 v138, v138, s65, v65
	v_med3_f32 v140, v140, s65, v65
	v_med3_f32 v142, v142, s65, v65
	v_med3_f32 v144, v144, s65, v65
	v_med3_f32 v146, v146, s65, v65
	v_med3_f32 v148, v148, s65, v65
	v_med3_f32 v150, v150, s65, v65
	v_cvt_pk_fp8_f32 v6, v93, v95 op_sel:[0,0,1]
	v_cvt_pk_fp8_f32 v7, v125, v127 op_sel:[0,0,1]
	v_cvt_pk_fp8_f32 v8, v129, v131 op_sel:[0,0,1]
	v_cvt_pk_fp8_f32 v9, v133, v135 op_sel:[0,0,1]
	v_med3_f32 v137, v137, s65, v65
	v_med3_f32 v139, v139, s65, v65
	v_med3_f32 v141, v141, s65, v65
	v_med3_f32 v143, v143, s65, v65
	v_med3_f32 v145, v145, s65, v65
	v_med3_f32 v147, v147, s65, v65
	v_med3_f32 v149, v149, s65, v65
	v_med3_f32 v151, v151, s65, v65
	v_cvt_pk_fp8_f32 v10, v136, v138 op_sel:[0,0,1]
	v_cvt_pk_fp8_f32 v11, v140, v142 op_sel:[0,0,1]
	v_cvt_pk_fp8_f32 v12, v144, v146 op_sel:[0,0,1]
	v_cvt_pk_fp8_f32 v13, v148, v150 op_sel:[0,0,1]
	v_cvt_pk_fp8_f32 v14, v137, v139 op_sel:[0,0,1]
	v_cvt_pk_fp8_f32 v15, v141, v143 op_sel:[0,0,1]
	v_cvt_pk_fp8_f32 v16, v145, v147 op_sel:[0,0,1]
	v_cvt_pk_fp8_f32 v17, v149, v151 op_sel:[0,0,1]
	global_store_dwordx4 v[32:33], v[2:5], off nt
	global_store_dwordx4 v[34:35], v[6:9], off nt
	global_store_dwordx4 v[36:37], v[10:13], off nt
	global_store_dwordx4 v[38:39], v[14:17], off nt
	s_waitcnt lgkmcnt(0)
	s_andn2_b64 exec, exec, s[16:17]
	s_cbranch_execnz .LBB0_12
	s_or_b64 exec, exec, s[16:17]
	s_lshl_b64 s[6:7], s[8:9], 11
	v_mad_u64_u32 v[28:29], s[0:1], s8, v67, v[26:27]
	s_mov_b64 s[14:15], 0
	v_mov_b32_e32 v30, v74
	v_mov_b32_e32 v86, v69
.LBB0_14:
	s_mov_b32 s0, 0x92492493
	v_mul_hi_i32 v32, v86, s0
	v_add_u32_e32 v32, v32, v86
	v_lshrrev_b32_e32 v33, 31, v32
	v_ashrrev_i32_e32 v32, 5, v32
	v_add_u32_e32 v33, v32, v33
	s_movk_i32 s0, 0xe400
	v_lshlrev_b32_e32 v32, 5, v33
	v_mad_u64_u32 v[34:35], s[0:1], v33, s0, v[30:31]
	v_ashrrev_i32_e32 v33, 31, v32
	v_add_u32_e32 v36, v34, v66
	v_ashrrev_i32_e32 v35, 31, v34
	v_lshl_add_u64 v[92:93], s[6:7], 0, v[32:33]
	v_lshl_add_u64 v[94:95], v[32:33], 2, v[28:29]
	v_ashrrev_i32_e32 v37, 31, v36
	v_add_u32_e32 v32, 8, v36
	v_add_u32_e32 v38, 16, v36
	v_add_u32_e32 v88, 24, v36
	v_add_u32_e32 v90, 32, v36
	v_add_u32_e32 v96, 40, v36
	v_add_u32_e32 v98, 48, v36
	v_add_u32_e32 v100, 56, v36
	v_add_u32_e32 v102, 64, v36
	v_add_u32_e32 v104, 0x48, v36
	v_add_u32_e32 v106, 0x50, v36
	v_add_u32_e32 v108, 0x58, v36
	v_add_u32_e32 v110, 0x60, v36
	v_add_u32_e32 v112, 0x68, v36
	v_add_u32_e32 v114, 0x70, v36
	v_add_u32_e32 v116, 0x78, v36
	v_lshl_add_u64 v[118:119], v[20:21], 0, v[34:35]
	v_lshlrev_b64 v[34:35], 13, v[36:37]
	v_ashrrev_i32_e32 v33, 31, v32
	v_ashrrev_i32_e32 v39, 31, v38
	v_ashrrev_i32_e32 v89, 31, v88
	v_ashrrev_i32_e32 v91, 31, v90
	v_ashrrev_i32_e32 v97, 31, v96
	v_ashrrev_i32_e32 v99, 31, v98
	v_ashrrev_i32_e32 v101, 31, v100
	v_ashrrev_i32_e32 v103, 31, v102
	v_ashrrev_i32_e32 v105, 31, v104
	v_ashrrev_i32_e32 v107, 31, v106
	v_ashrrev_i32_e32 v109, 31, v108
	v_ashrrev_i32_e32 v111, 31, v110
	v_ashrrev_i32_e32 v113, 31, v112
	v_ashrrev_i32_e32 v115, 31, v114
	v_ashrrev_i32_e32 v117, 31, v116
	v_or_b32_e32 v36, v92, v66
	v_or_b32_e32 v37, v92, v68
	v_or_b32_e32 v87, v92, v70
	v_or_b32_e32 v92, v92, v72
	v_lshl_add_u64 v[120:121], v[94:95], 0, v[34:35]
	v_lshlrev_b64 v[122:123], 13, v[32:33]
	v_lshlrev_b64 v[124:125], 13, v[38:39]
	v_lshlrev_b64 v[126:127], 13, v[88:89]
	v_lshlrev_b64 v[128:129], 13, v[90:91]
	v_lshlrev_b64 v[96:97], 13, v[96:97]
	v_lshlrev_b64 v[98:99], 13, v[98:99]
	v_lshlrev_b64 v[100:101], 13, v[100:101]
	v_lshlrev_b64 v[102:103], 13, v[102:103]
	v_lshlrev_b64 v[104:105], 13, v[104:105]
	v_lshlrev_b64 v[106:107], 13, v[106:107]
	v_lshlrev_b64 v[108:109], 13, v[108:109]
	v_lshlrev_b64 v[110:111], 13, v[110:111]
	v_lshlrev_b64 v[112:113], 13, v[112:113]
	v_lshlrev_b64 v[114:115], 13, v[114:115]
	v_lshlrev_b64 v[116:117], 13, v[116:117]
	v_mad_u64_u32 v[38:39], s[0:1], v36, s21, v[118:119]
	v_mad_u64_u32 v[36:37], s[0:1], v37, s21, v[118:119]
	v_mad_u64_u32 v[34:35], s[0:1], v87, s21, v[118:119]
	v_mad_u64_u32 v[32:33], s[0:1], v92, s21, v[118:119]
	global_load_dwordx4 v[88:91], v[120:121], off nt
	v_lshl_add_u64 v[118:119], v[94:95], 0, v[122:123]
	v_lshl_add_u64 v[120:121], v[94:95], 0, v[124:125]
	v_lshl_add_u64 v[122:123], v[94:95], 0, v[126:127]
	v_lshl_add_u64 v[124:125], v[94:95], 0, v[128:129]
	v_lshl_add_u64 v[126:127], v[94:95], 0, v[96:97]
	v_lshl_add_u64 v[128:129], v[94:95], 0, v[98:99]
	v_lshl_add_u64 v[130:131], v[94:95], 0, v[100:101]
	v_lshl_add_u64 v[132:133], v[94:95], 0, v[102:103]
	v_lshl_add_u64 v[134:135], v[94:95], 0, v[104:105]
	v_lshl_add_u64 v[136:137], v[94:95], 0, v[106:107]
	v_lshl_add_u64 v[138:139], v[94:95], 0, v[108:109]
	v_lshl_add_u64 v[140:141], v[94:95], 0, v[110:111]
	v_lshl_add_u64 v[142:143], v[94:95], 0, v[112:113]
	v_lshl_add_u64 v[144:145], v[94:95], 0, v[114:115]
	v_lshl_add_u64 v[148:149], v[94:95], 0, v[116:117]
	v_mad_i32_i24 v39, v93, s21, v39
	v_mad_i32_i24 v37, v93, s21, v37
	v_mad_i32_i24 v35, v93, s21, v35
	v_mad_i32_i24 v33, v93, s21, v33
	global_load_dwordx4 v[92:95], v[118:119], off nt
	global_load_dwordx4 v[96:99], v[120:121], off nt
	global_load_dwordx4 v[100:103], v[122:123], off nt
	global_load_dwordx4 v[104:107], v[124:125], off nt
	global_load_dwordx4 v[108:111], v[126:127], off nt
	global_load_dwordx4 v[112:115], v[128:129], off nt
	global_load_dwordx4 v[116:119], v[130:131], off nt
	s_nop 0
	global_load_dwordx4 v[120:123], v[132:133], off nt
	global_load_dwordx4 v[124:127], v[134:135], off nt
	global_load_dwordx4 v[128:131], v[136:137], off nt
	s_nop 0
	global_load_dwordx4 v[132:135], v[138:139], off nt
	s_nop 0
	global_load_dwordx4 v[136:139], v[140:141], off nt
	s_nop 0
	global_load_dwordx4 v[140:143], v[142:143], off nt
	s_nop 0
	global_load_dwordx4 v[144:147], v[144:145], off nt
	s_nop 0
	global_load_dwordx4 v[148:151], v[148:149], off nt
	s_waitcnt vmcnt(15)
	ds_write2_b32 v40, v88, v89 offset1:1
	ds_write2_b32 v40, v90, v91 offset0:2 offset1:3
	s_waitcnt vmcnt(14)
	ds_write2_b32 v41, v92, v93 offset1:1
	ds_write2_b32 v42, v94, v95 offset1:1
	s_waitcnt vmcnt(13)
	ds_write2_b32 v43, v96, v97 offset1:1
	ds_write2_b32 v44, v98, v99 offset1:1
	s_waitcnt vmcnt(12)
	ds_write2_b32 v45, v100, v101 offset1:1
	ds_write2_b32 v46, v102, v103 offset1:1
	s_waitcnt vmcnt(11)
	ds_write2_b32 v47, v104, v105 offset1:1
	ds_write2_b32 v48, v106, v107 offset1:1
	s_waitcnt vmcnt(10)
	ds_write2_b32 v49, v108, v109 offset1:1
	ds_write2_b32 v50, v110, v111 offset1:1
	s_waitcnt vmcnt(9)
	ds_write2_b32 v51, v112, v113 offset1:1
	ds_write2_b32 v52, v114, v115 offset1:1
	s_waitcnt vmcnt(8)
	ds_write2_b32 v53, v116, v117 offset1:1
	ds_write2_b32 v54, v118, v119 offset1:1
	s_waitcnt vmcnt(7)
	ds_write2_b32 v55, v120, v121 offset1:1
	ds_write2_b32 v56, v122, v123 offset1:1
	s_waitcnt vmcnt(6)
	ds_write2_b32 v57, v124, v125 offset1:1
	ds_write2_b32 v58, v126, v127 offset1:1
	s_waitcnt vmcnt(5)
	ds_write2_b32 v59, v128, v129 offset1:1
	ds_write2_b32 v60, v130, v131 offset1:1
	s_waitcnt vmcnt(4)
	ds_write2_b32 v61, v132, v133 offset1:1
	ds_write2_b32 v62, v134, v135 offset1:1
	s_waitcnt vmcnt(3)
	ds_write2_b32 v63, v136, v137 offset1:1
	ds_write2_b32 v64, v138, v139 offset1:1
	s_waitcnt vmcnt(2)
	ds_write2_b32 v71, v140, v141 offset1:1
	ds_write2_b32 v73, v142, v143 offset1:1
	s_waitcnt vmcnt(1)
	ds_write2_b32 v76, v144, v145 offset1:1
	ds_write2_b32 v77, v146, v147 offset1:1
	s_waitcnt vmcnt(0)
	ds_write2_b32 v82, v148, v149 offset1:1
	ds_write2_b32 v83, v150, v151 offset1:1
	s_waitcnt lgkmcnt(0)
	ds_read2_b32 v[88:89], v75 offset1:8
	ds_read2_b32 v[90:91], v75 offset0:33 offset1:41
	ds_read2_b32 v[92:93], v75 offset0:66 offset1:74
	ds_read2_b32 v[94:95], v75 offset0:99 offset1:107
	ds_read2_b32 v[96:97], v75 offset0:132 offset1:140
	ds_read2_b32 v[98:99], v75 offset0:165 offset1:173
	ds_read2_b32 v[100:101], v75 offset0:198 offset1:206
	ds_read2_b32 v[102:103], v75 offset0:231 offset1:239
	ds_read2_b32 v[104:105], v84 offset0:8 offset1:16
	ds_read2_b32 v[106:107], v84 offset0:41 offset1:49
	ds_read2_b32 v[108:109], v84 offset0:74 offset1:82
	ds_read2_b32 v[110:111], v84 offset0:107 offset1:115
	ds_read2_b32 v[112:113], v84 offset0:140 offset1:148
	ds_read2_b32 v[114:115], v84 offset0:173 offset1:181
	ds_read2_b32 v[116:117], v84 offset0:206 offset1:214
	ds_read2_b32 v[118:119], v84 offset0:239 offset1:247
	ds_read2_b32 v[120:121], v75 offset0:16 offset1:24
	ds_read2_b32 v[122:123], v75 offset0:49 offset1:57
	ds_read2_b32 v[124:125], v75 offset0:82 offset1:90
	ds_read2_b32 v[126:127], v75 offset0:115 offset1:123
	ds_read2_b32 v[128:129], v75 offset0:148 offset1:156
	ds_read2_b32 v[130:131], v75 offset0:181 offset1:189
	ds_read2_b32 v[132:133], v75 offset0:214 offset1:222
	ds_read2_b32 v[134:135], v75 offset0:247 offset1:255
	ds_read2_b32 v[136:137], v84 offset0:24 offset1:32
	ds_read2_b32 v[138:139], v84 offset0:57 offset1:65
	ds_read2_b32 v[140:141], v84 offset0:90 offset1:98
	ds_read2_b32 v[142:143], v84 offset0:123 offset1:131
	ds_read2_b32 v[144:145], v84 offset0:156 offset1:164
	ds_read2_b32 v[146:147], v84 offset0:189 offset1:197
	ds_read2_b32 v[148:149], v84 offset0:222 offset1:230
	ds_read2_b32 v[150:151], v85 offset0:127 offset1:135
	s_waitcnt lgkmcnt(14)
	v_mul_f32_e32 v87, 0x43800000, v88
	v_mul_f32_e32 v88, 0x43800000, v90
	v_mul_f32_e32 v90, 0x43800000, v92
	v_mul_f32_e32 v92, 0x43800000, v94
	v_mul_f32_e32 v94, 0x43800000, v96
	v_mul_f32_e32 v96, 0x43800000, v98
	v_mul_f32_e32 v98, 0x43800000, v100
	v_mul_f32_e32 v100, 0x43800000, v102
	v_mul_f32_e32 v102, 0x43800000, v104
	v_mul_f32_e32 v104, 0x43800000, v106
	v_mul_f32_e32 v106, 0x43800000, v108
	v_mul_f32_e32 v108, 0x43800000, v110
	v_mul_f32_e32 v110, 0x43800000, v112
	v_mul_f32_e32 v112, 0x43800000, v114
	v_mov_b32_e32 v2, 0
	v_mov_b32_e32 v3, 0
	v_mov_b32_e32 v4, 0
	v_mov_b32_e32 v5, 0
	v_mul_f32_e32 v89, 0x43800000, v89
	v_mul_f32_e32 v91, 0x43800000, v91
	v_mul_f32_e32 v97, 0x43800000, v97
	v_mul_f32_e32 v99, 0x43800000, v99
	v_mul_f32_e32 v105, 0x43800000, v105
	v_mul_f32_e32 v107, 0x43800000, v107
	v_mul_f32_e32 v113, 0x43800000, v113
	v_mul_f32_e32 v115, 0x43800000, v115
	v_med3_f32 v87, v87, s65, v65
	v_med3_f32 v88, v88, s65, v65
	v_med3_f32 v94, v94, s65, v65
	v_med3_f32 v96, v96, s65, v65
	v_med3_f32 v102, v102, s65, v65
	v_med3_f32 v104, v104, s65, v65
	v_med3_f32 v110, v110, s65, v65
	v_med3_f32 v112, v112, s65, v65
	v_mov_b32_e32 v6, 0
	v_mov_b32_e32 v7, 0
	v_mov_b32_e32 v8, 0
	v_mov_b32_e32 v9, 0
	v_mul_f32_e32 v114, 0x43800000, v116
	v_mul_f32_e32 v116, 0x43800000, v118
	v_mul_f32_e32 v118, 0x43800000, v119
	v_mul_f32_e32 v119, 0x43800000, v120
	v_mul_f32_e32 v120, 0x43800000, v122
	s_waitcnt lgkmcnt(13)
	v_mul_f32_e32 v122, 0x43800000, v124
	s_waitcnt lgkmcnt(12)
	v_mul_f32_e32 v124, 0x43800000, v126
	s_waitcnt lgkmcnt(11)
	v_mul_f32_e32 v126, 0x43800000, v128
	s_waitcnt lgkmcnt(10)
	v_mul_f32_e32 v128, 0x43800000, v130
	s_waitcnt lgkmcnt(9)
	v_mul_f32_e32 v130, 0x43800000, v132
	s_waitcnt lgkmcnt(8)
	v_mul_f32_e32 v132, 0x43800000, v134
	s_waitcnt lgkmcnt(7)
	v_mul_f32_e32 v134, 0x43800000, v136
	s_waitcnt lgkmcnt(6)
	v_mul_f32_e32 v136, 0x43800000, v138
	s_waitcnt lgkmcnt(5)
	v_mul_f32_e32 v138, 0x43800000, v140
	s_waitcnt lgkmcnt(4)
	v_mul_f32_e32 v140, 0x43800000, v142
	s_waitcnt lgkmcnt(3)
	v_mul_f32_e32 v142, 0x43800000, v144
	s_waitcnt lgkmcnt(2)
	v_mul_f32_e32 v144, 0x43800000, v146
	v_med3_f32 v89, v89, s65, v65
	v_med3_f32 v91, v91, s65, v65
	v_med3_f32 v97, v97, s65, v65
	v_med3_f32 v99, v99, s65, v65
	v_med3_f32 v105, v105, s65, v65
	v_med3_f32 v107, v107, s65, v65
	v_med3_f32 v113, v113, s65, v65
	v_med3_f32 v115, v115, s65, v65
	v_cvt_pk_fp8_f32 v2, v87, v88
	v_cvt_pk_fp8_f32 v3, v94, v96
	v_cvt_pk_fp8_f32 v4, v102, v104
	v_cvt_pk_fp8_f32 v5, v110, v112
	v_mov_b32_e32 v10, 0
	v_mov_b32_e32 v11, 0
	v_mov_b32_e32 v12, 0
	v_mov_b32_e32 v13, 0
	v_mul_f32_e32 v121, 0x43800000, v121
	v_mul_f32_e32 v123, 0x43800000, v123
	v_mul_f32_e32 v129, 0x43800000, v129
	v_mul_f32_e32 v131, 0x43800000, v131
	v_mul_f32_e32 v137, 0x43800000, v137
	v_mul_f32_e32 v139, 0x43800000, v139
	v_mul_f32_e32 v145, 0x43800000, v145
	v_mul_f32_e32 v147, 0x43800000, v147
	v_med3_f32 v119, v119, s65, v65
	v_med3_f32 v120, v120, s65, v65
	v_med3_f32 v126, v126, s65, v65
	v_med3_f32 v128, v128, s65, v65
	v_med3_f32 v134, v134, s65, v65
	v_med3_f32 v136, v136, s65, v65
	v_med3_f32 v142, v142, s65, v65
	v_med3_f32 v144, v144, s65, v65
	v_cvt_pk_fp8_f32 v6, v89, v91
	v_cvt_pk_fp8_f32 v7, v97, v99
	v_cvt_pk_fp8_f32 v8, v105, v107
	v_cvt_pk_fp8_f32 v9, v113, v115
	v_mov_b32_e32 v14, 0
	v_mov_b32_e32 v15, 0
	v_mov_b32_e32 v16, 0
	v_mov_b32_e32 v17, 0
	v_med3_f32 v121, v121, s65, v65
	v_med3_f32 v123, v123, s65, v65
	v_med3_f32 v129, v129, s65, v65
	v_med3_f32 v131, v131, s65, v65
	v_med3_f32 v137, v137, s65, v65
	v_med3_f32 v139, v139, s65, v65
	v_med3_f32 v145, v145, s65, v65
	v_med3_f32 v147, v147, s65, v65
	v_cvt_pk_fp8_f32 v10, v119, v120
	v_cvt_pk_fp8_f32 v11, v126, v128
	v_cvt_pk_fp8_f32 v12, v134, v136
	v_cvt_pk_fp8_f32 v13, v142, v144
	v_mul_f32_e32 v93, 0x43800000, v93
	v_mul_f32_e32 v95, 0x43800000, v95
	v_mul_f32_e32 v101, 0x43800000, v101
	v_mul_f32_e32 v103, 0x43800000, v103
	v_mul_f32_e32 v109, 0x43800000, v109
	v_mul_f32_e32 v111, 0x43800000, v111
	v_mul_f32_e32 v117, 0x43800000, v117
	v_med3_f32 v90, v90, s65, v65
	v_med3_f32 v92, v92, s65, v65
	v_med3_f32 v98, v98, s65, v65
	v_med3_f32 v100, v100, s65, v65
	v_med3_f32 v106, v106, s65, v65
	v_med3_f32 v108, v108, s65, v65
	v_med3_f32 v114, v114, s65, v65
	v_med3_f32 v116, v116, s65, v65
	v_cvt_pk_fp8_f32 v14, v121, v123
	v_cvt_pk_fp8_f32 v15, v129, v131
	v_cvt_pk_fp8_f32 v16, v137, v139
	v_cvt_pk_fp8_f32 v17, v145, v147
	s_waitcnt lgkmcnt(1)
	v_mul_f32_e32 v146, 0x43800000, v148
	v_mul_f32_e32 v148, 0x43800000, v149
	s_waitcnt lgkmcnt(0)
	v_mul_f32_e32 v149, 0x43800000, v150
	v_med3_f32 v93, v93, s65, v65
	v_med3_f32 v95, v95, s65, v65
	v_med3_f32 v101, v101, s65, v65
	v_med3_f32 v103, v103, s65, v65
	v_med3_f32 v109, v109, s65, v65
	v_med3_f32 v111, v111, s65, v65
	v_med3_f32 v117, v117, s65, v65
	v_med3_f32 v118, v118, s65, v65
	v_cvt_pk_fp8_f32 v2, v90, v92 op_sel:[0,0,1]
	v_cvt_pk_fp8_f32 v3, v98, v100 op_sel:[0,0,1]
	v_cvt_pk_fp8_f32 v4, v106, v108 op_sel:[0,0,1]
	v_cvt_pk_fp8_f32 v5, v114, v116 op_sel:[0,0,1]
	v_mul_f32_e32 v125, 0x43800000, v125
	v_mul_f32_e32 v127, 0x43800000, v127
	v_mul_f32_e32 v133, 0x43800000, v133
	v_mul_f32_e32 v135, 0x43800000, v135
	v_mul_f32_e32 v141, 0x43800000, v141
	v_mul_f32_e32 v143, 0x43800000, v143
	v_mul_f32_e32 v150, 0x43800000, v151
	v_med3_f32 v122, v122, s65, v65
	v_med3_f32 v124, v124, s65, v65
	v_med3_f32 v130, v130, s65, v65
	v_med3_f32 v132, v132, s65, v65
	v_med3_f32 v138, v138, s65, v65
	v_med3_f32 v140, v140, s65, v65
	v_med3_f32 v146, v146, s65, v65
	v_med3_f32 v149, v149, s65, v65
	v_cvt_pk_fp8_f32 v6, v93, v95 op_sel:[0,0,1]
	v_cvt_pk_fp8_f32 v7, v101, v103 op_sel:[0,0,1]
	v_cvt_pk_fp8_f32 v8, v109, v111 op_sel:[0,0,1]
	v_cvt_pk_fp8_f32 v9, v117, v118 op_sel:[0,0,1]
	v_med3_f32 v125, v125, s65, v65
	v_med3_f32 v127, v127, s65, v65
	v_med3_f32 v133, v133, s65, v65
	v_med3_f32 v135, v135, s65, v65
	v_med3_f32 v141, v141, s65, v65
	v_med3_f32 v143, v143, s65, v65
	v_med3_f32 v148, v148, s65, v65
	v_med3_f32 v150, v150, s65, v65
	v_cvt_pk_fp8_f32 v10, v122, v124 op_sel:[0,0,1]
	v_cvt_pk_fp8_f32 v11, v130, v132 op_sel:[0,0,1]
	v_cvt_pk_fp8_f32 v12, v138, v140 op_sel:[0,0,1]
	v_cvt_pk_fp8_f32 v13, v146, v149 op_sel:[0,0,1]
	v_cvt_pk_fp8_f32 v14, v125, v127 op_sel:[0,0,1]
	v_cvt_pk_fp8_f32 v15, v133, v135 op_sel:[0,0,1]
	v_cvt_pk_fp8_f32 v16, v141, v143 op_sel:[0,0,1]
	v_cvt_pk_fp8_f32 v17, v148, v150 op_sel:[0,0,1]
	global_store_dwordx4 v[38:39], v[2:5], off nt
	global_store_dwordx4 v[36:37], v[6:9], off nt
	global_store_dwordx4 v[34:35], v[10:13], off nt
	global_store_dwordx4 v[32:33], v[14:17], off nt
	v_add_u32_e32 v86, s3, v86
	s_waitcnt lgkmcnt(0)
	v_cmp_lt_i32_e64 s[0:1], s66, v86
	s_or_b64 s[14:15], s[0:1], s[14:15]
	v_add_u32_e32 v30, s67, v30
	s_andn2_b64 exec, exec, s[14:15]
	s_cbranch_execnz .LBB0_14
	s_branch .LBB0_7
